# adds: prologue B row loads batched (12 loads in flight per row)
# baseline (speedup 1.0000x reference)
; #define GAS __attribute__((address_space(1)))
; __device__ __forceinline__ unsigned pk2(float lo, float hi) { const f32x2cv v = {lo, hi}; return __builtin_bit_cast(unsigned, __builtin_convertvector(v, bf16x2cv)); }
; __device__ __forceinline__ const float* modv(const Frame& F, int l, int r, int k) { return (const float*)(F.ws + WS_MODV) + ((size_t)(l * 9 + r) * 6 + k) * 1024; }
; __device__ __forceinline__ void modulate_row_bf16(const Frame& F, const float* hrow, const float* sh, const float* sc, bf16* orow, bf16* hbrow) {
;     const GAS f32x4* xr = (const GAS f32x4*)hrow + F.lane; const f32x4* shv = (const f32x4*)sh + F.lane; const f32x4* scv = (const f32x4*)sc + F.lane;
;     GAS v2u* o8 = (GAS v2u*)orow + F.lane; GAS v2u* h8 = (GAS v2u*)hbrow + F.lane;
; #pragma unroll
;     for (int j = 0; j < 4; ++j) { const f32x4 v = __builtin_nontemporal_load((const f32x4*)hrow + F.lane + 64 * j)  , a = shv[64 * j], b = scv[64 * j]; const f32x4 y = v * (b + 1.0f) + a; v2u o; o.x = pk2(y.x, y.y); o.y = pk2(y.z, y.w); o8[64 * j] = o;
;         v2u hq; hq.x = pk2(v.x, v.y); hq.y = pk2(v.z, v.w); h8[64 * j] = hq; }
; }
; __device__ __forceinline__ void phase_prologue_b(Frame& F0, const Args& A) {
;     Frame F = fresh(F0);
;     const int gw = F.vcu * NWAVES + F.wave, NGW = F.G * NWAVES;
;     for (int R = gw; R < M; R += NGW) { const int mr = modrow_of(R);
;         const float* src = R < ML ? A.in[I_X + F.z] + (size_t)R * D : A.in[I_CTX + F.z] + (size_t)(R - ML) * D;
;         modulate_row_bf16(F, src, modv(F, 0, mr, 0), modv(F, 0, mr, 1), (bf16*)(F.ws + WS_ABUF) + (size_t)R * D, (bf16*)(F.ws + WS_HB) + (size_t)R * D); }
.LBB0_107:
	s_min_i32 s2, s0, 0x8000
	s_ashr_i32 s2, s2, 12
	s_mul_i32 s18, s2, 6
	s_ashr_i32 s19, s18, 31
	s_lshl_b64 s[18:19], s[18:19], 12
	s_add_u32 s24, s6, s18
	s_addc_u32 s25, s7, s19
	v_lshl_add_u64 v[24:25], s[24:25], 0, v[6:7]
	v_lshl_add_u64 v[22:23], s[16:17], 0, v[6:7]
	v_lshl_add_u64 v[20:21], v[24:25], 0, s[12:13]
	s_lshl_b64 s[14:15], s[14:15], 11
	v_lshl_add_u64 v[26:27], v[2:3], 0, s[14:15]
	v_lshl_add_u64 v[28:29], v[4:5], 0, s[14:15]
	global_load_dwordx4 v[48:51], v[20:21], off
	global_load_dwordx4 v[32:35], v[22:23], off nt
	global_load_dwordx4 v[64:67], v[24:25], off
	global_load_dwordx4 v[52:55], v[20:21], off offset:1024
	global_load_dwordx4 v[36:39], v[22:23], off offset:1024 nt
	global_load_dwordx4 v[68:71], v[24:25], off offset:1024
	global_load_dwordx4 v[56:59], v[20:21], off offset:2048
	global_load_dwordx4 v[40:43], v[22:23], off offset:2048 nt
	global_load_dwordx4 v[72:75], v[24:25], off offset:2048
	global_load_dwordx4 v[60:63], v[20:21], off offset:3072
	global_load_dwordx4 v[44:47], v[22:23], off offset:3072 nt
	global_load_dwordx4 v[76:79], v[24:25], off offset:3072
	s_add_u32 s0, s0, s52
	s_addc_u32 s1, s1, s53
	s_add_u32 s8, s8, s10
	s_addc_u32 s9, s9, s11
	s_cmp_lt_i32 s0, 0x8800
	s_waitcnt vmcnt(9)
	v_pk_add_f32 v[50:51], v[50:51], 1.0 op_sel_hi:[1,0]
	v_pk_add_f32 v[48:49], v[48:49], 1.0 op_sel_hi:[1,0]
	v_cvt_pk_bf16_f32 v80, v32, v33
	v_cvt_pk_bf16_f32 v81, v34, v35
	v_pk_fma_f32 v[34:35], v[34:35], v[50:51], v[66:67]
	v_pk_fma_f32 v[32:33], v[32:33], v[48:49], v[64:65]
	global_store_dwordx2 v[28:29], v[80:81], off
	v_cvt_pk_bf16_f32 v88, v32, v33
	v_cvt_pk_bf16_f32 v89, v34, v35
	global_store_dwordx2 v[26:27], v[88:89], off
	s_waitcnt vmcnt(8)
	v_pk_add_f32 v[54:55], v[54:55], 1.0 op_sel_hi:[1,0]
	v_pk_add_f32 v[52:53], v[52:53], 1.0 op_sel_hi:[1,0]
	v_cvt_pk_bf16_f32 v82, v36, v37
	v_cvt_pk_bf16_f32 v83, v38, v39
	v_pk_fma_f32 v[38:39], v[38:39], v[54:55], v[70:71]
	v_pk_fma_f32 v[36:37], v[36:37], v[52:53], v[68:69]
	global_store_dwordx2 v[28:29], v[82:83], off offset:512
	v_cvt_pk_bf16_f32 v90, v36, v37
	v_cvt_pk_bf16_f32 v91, v38, v39
	global_store_dwordx2 v[26:27], v[90:91], off offset:512
	s_waitcnt vmcnt(7)
	v_pk_add_f32 v[58:59], v[58:59], 1.0 op_sel_hi:[1,0]
	v_pk_add_f32 v[56:57], v[56:57], 1.0 op_sel_hi:[1,0]
	v_cvt_pk_bf16_f32 v84, v40, v41
	v_cvt_pk_bf16_f32 v85, v42, v43
	v_pk_fma_f32 v[42:43], v[42:43], v[58:59], v[74:75]
	v_pk_fma_f32 v[40:41], v[40:41], v[56:57], v[72:73]
	global_store_dwordx2 v[28:29], v[84:85], off offset:1024
	v_cvt_pk_bf16_f32 v92, v40, v41
	v_cvt_pk_bf16_f32 v93, v42, v43
	global_store_dwordx2 v[26:27], v[92:93], off offset:1024
	s_waitcnt vmcnt(6)
	v_pk_add_f32 v[62:63], v[62:63], 1.0 op_sel_hi:[1,0]
	v_pk_add_f32 v[60:61], v[60:61], 1.0 op_sel_hi:[1,0]
	v_cvt_pk_bf16_f32 v86, v44, v45
	v_cvt_pk_bf16_f32 v87, v46, v47
	v_pk_fma_f32 v[46:47], v[46:47], v[62:63], v[78:79]
	v_pk_fma_f32 v[44:45], v[44:45], v[60:61], v[76:77]
	global_store_dwordx2 v[28:29], v[86:87], off offset:1536
	v_cvt_pk_bf16_f32 v94, v44, v45
	v_cvt_pk_bf16_f32 v95, v46, v47
	global_store_dwordx2 v[26:27], v[94:95], off offset:1536
	s_cbranch_scc0 .LBB0_112
